# baseline (speedup 1.0000x reference)
.LBB1_8:
	s_or_b64 exec, exec, s[4:5]
	s_waitcnt vmcnt(1)
	v_mov_b32_e32 v184, 1
	v_lshl_add_u32 v180, v176, 2, v172
	v_lshl_add_u32 v181, v177, 2, v172
	v_lshl_add_u32 v182, v178, 2, v172
	v_lshl_add_u32 v183, v179, 2, v172
	s_waitcnt lgkmcnt(0)
	ds_add_u32 v180, v184
	ds_add_u32 v181, v184
	ds_add_u32 v182, v184
	ds_add_u32 v183, v184
	s_waitcnt lgkmcnt(0)
	ds_read_b32 v151, v173
	s_waitcnt lgkmcnt(0)
	v_cvt_f32_i32_e32 v185, v151
	ds_write_b32 v173, v185 offset:256
	v_add_u32_e32 v10, v172, v2
	s_waitcnt vmcnt(1) lgkmcnt(0)
	s_barrier
	s_nop 0
	s_nop 0
	s_nop 0
	s_nop 0
	ds_read_b128 v[18:21], v10 offset:256
	ds_read_b128 v[22:25], v10 offset:288
	ds_read_b128 v[82:85], v10 offset:320
	ds_read_b128 v[86:89], v10 offset:352
	ds_read_b128 v[74:77], v10 offset:384
	ds_read_b128 v[78:81], v10 offset:416
	ds_read_b128 v[2:5], v213 offset:32768
	ds_read_b128 v[6:9], v213 offset:0
	ds_read_b128 v[66:69], v10 offset:448
	ds_read_b128 v[70:73], v10 offset:480
	ds_read_b128 v[10:13], v213 offset:1024
	s_waitcnt lgkmcnt(3)
	v_pk_mul_f32 v[26:27], v[8:9], v[20:21]
	v_pk_mul_f32 v[28:29], v[6:7], v[18:19]
	ds_read_b128 v[14:17], v213 offset:8192
	s_waitcnt lgkmcnt(1)
	v_pk_mul_f32 v[12:13], v[12:13], v[24:25]
	v_pk_mul_f32 v[10:11], v[10:11], v[22:23]
	v_pk_fma_f32 v[30:31], v[8:9], v[20:21], v[12:13]
	v_pk_fma_f32 v[32:33], v[6:7], v[18:19], v[10:11]
	v_cvt_pk_bf16_f32 v9, v12, v13
	v_cvt_pk_bf16_f32 v7, v26, v27
	v_cvt_pk_bf16_f32 v8, v10, v11
	v_cvt_pk_bf16_f32 v6, v28, v29
	ds_read_b128 v[10:13], v213 offset:33792
	s_nop 0
	v_mfma_f32_32x32x16_bf16 v[34:49], v[2:5], v[6:9], 0
	ds_read_b128 v[6:9], v213 offset:9216
	s_waitcnt lgkmcnt(2)
	v_mul_f32_e32 v26, v16, v20
	v_mul_f32_e32 v27, v17, v21
	v_pk_mul_f32 v[50:51], v[14:15], v[18:19]
	s_mov_b32 s4, 0x3727c5ac
	s_waitcnt lgkmcnt(0)
	v_pk_mul_f32 v[8:9], v[8:9], v[24:25]
	v_pk_mul_f32 v[28:29], v[6:7], v[22:23]
	v_pk_fma_f32 v[90:91], v[16:17], v[20:21], v[8:9]
	v_pk_fma_f32 v[92:93], v[14:15], v[18:19], v[28:29]
	ds_read_b128 v[14:17], v213 offset:2048
	v_cvt_pk_bf16_f32 v9, v8, v9
	v_cvt_pk_bf16_f32 v7, v26, v27
	v_cvt_pk_bf16_f32 v8, v28, v29
	ds_read_b128 v[26:29], v213 offset:3072
	v_cvt_pk_bf16_f32 v6, v50, v51
	s_waitcnt lgkmcnt(1)
	v_pk_mul_f32 v[94:95], v[14:15], v[82:83]
	s_mov_b32 s0, 0x3c800000
	v_mfma_f32_32x32x16_bf16 v[50:65], v[2:5], v[6:9], 0
	v_mul_f32_e32 v2, v16, v84
	v_mul_f32_e32 v3, v17, v85
	s_waitcnt lgkmcnt(0)
	v_mul_f32_e32 v4, v28, v88
	v_mul_f32_e32 v5, v29, v89
	v_pk_mul_f32 v[6:7], v[26:27], v[86:87]
	v_pk_fma_f32 v[8:9], v[16:17], v[84:85], v[4:5]
	v_cvt_pk_bf16_f32 v3, v2, v3
	v_pk_fma_f32 v[14:15], v[14:15], v[82:83], v[6:7]
	v_pk_add_f32 v[26:27], v[8:9], v[30:31]
	v_cvt_pk_bf16_f32 v5, v4, v5
	v_cvt_pk_bf16_f32 v4, v6, v7
	ds_read_b128 v[6:9], v213 offset:10240
	v_pk_add_f32 v[28:29], v[14:15], v[32:33]
	ds_read_b128 v[14:17], v213 offset:11264
	v_cvt_pk_bf16_f32 v2, v94, v95
	s_waitcnt lgkmcnt(1)
	v_pk_mul_f32 v[30:31], v[6:7], v[82:83]
	v_mov_b64_e32 v[152:153], s[4:5]
	v_mfma_f32_32x32x16_bf16 v[34:49], v[10:13], v[2:5], v[34:49]
	v_mul_f32_e32 v2, v8, v84
	v_mul_f32_e32 v3, v9, v85
	s_waitcnt lgkmcnt(0)
	v_mul_f32_e32 v4, v16, v88
	v_mul_f32_e32 v5, v17, v89
	v_pk_mul_f32 v[14:15], v[14:15], v[86:87]
	v_pk_fma_f32 v[8:9], v[8:9], v[84:85], v[4:5]
	v_pk_fma_f32 v[6:7], v[6:7], v[82:83], v[14:15]
	v_cvt_pk_bf16_f32 v5, v4, v5
	v_cvt_pk_bf16_f32 v3, v2, v3
	v_cvt_pk_bf16_f32 v4, v14, v15
	v_pk_add_f32 v[32:33], v[8:9], v[90:91]
	v_pk_add_f32 v[90:91], v[6:7], v[92:93]
	ds_read_b128 v[6:9], v213 offset:34816
	ds_read_b128 v[14:17], v213 offset:4096
	v_cvt_pk_bf16_f32 v2, v30, v31
	s_mov_b32 s13, 0
	s_mov_b64 s[6:7], 0
	v_mfma_f32_32x32x16_bf16 v[50:65], v[10:13], v[2:5], v[50:65]
	ds_read_b128 v[2:5], v213 offset:5120
	ds_read_b128 v[10:13], v213 offset:12288
	s_waitcnt lgkmcnt(2)
	v_pk_mul_f32 v[30:31], v[16:17], v[76:77]
	v_pk_mul_f32 v[92:93], v[14:15], v[74:75]
	s_waitcnt lgkmcnt(1)
	v_pk_mul_f32 v[4:5], v[4:5], v[80:81]
	v_pk_mul_f32 v[94:95], v[2:3], v[78:79]
	v_pk_fma_f32 v[2:3], v[16:17], v[76:77], v[4:5]
	v_cvt_pk_bf16_f32 v5, v4, v5
	v_pk_add_f32 v[96:97], v[2:3], v[26:27]
	v_cvt_pk_bf16_f32 v3, v30, v31
	v_cvt_pk_bf16_f32 v4, v94, v95
	v_cvt_pk_bf16_f32 v2, v92, v93
	v_pk_fma_f32 v[14:15], v[14:15], v[74:75], v[94:95]
	s_waitcnt lgkmcnt(0)
	v_pk_mul_f32 v[30:31], v[10:11], v[74:75]
	v_mfma_f32_32x32x16_bf16 v[34:49], v[6:9], v[2:5], v[34:49]
	ds_read_b128 v[2:5], v213 offset:13312
	v_add_f32_e32 v98, v14, v28
	v_add_f32_e32 v99, v15, v29
	ds_read_b128 v[14:17], v213 offset:35840
	v_pk_mul_f32 v[26:27], v[12:13], v[76:77]
	s_waitcnt lgkmcnt(1)
	v_pk_mul_f32 v[4:5], v[4:5], v[80:81]
	v_pk_mul_f32 v[28:29], v[2:3], v[78:79]
	v_pk_fma_f32 v[2:3], v[12:13], v[76:77], v[4:5]
	v_pk_fma_f32 v[10:11], v[10:11], v[74:75], v[28:29]
	v_pk_add_f32 v[32:33], v[2:3], v[32:33]
	v_pk_add_f32 v[92:93], v[10:11], v[90:91]
	ds_read_b128 v[10:13], v213 offset:6144
	v_cvt_pk_bf16_f32 v5, v4, v5
	v_cvt_pk_bf16_f32 v3, v26, v27
	v_cvt_pk_bf16_f32 v4, v28, v29
	ds_read_b128 v[26:29], v213 offset:7168
	v_cvt_pk_bf16_f32 v2, v30, v31
	s_waitcnt lgkmcnt(1)
	v_pk_mul_f32 v[30:31], v[10:11], v[66:67]
	v_mfma_f32_32x32x16_bf16 v[50:65], v[6:9], v[2:5], v[50:65]
	v_mul_f32_e32 v2, v12, v68
	v_mul_f32_e32 v3, v13, v69
	s_waitcnt lgkmcnt(0)
	v_mul_f32_e32 v4, v28, v72
	v_mul_f32_e32 v5, v29, v73
	v_pk_mul_f32 v[6:7], v[26:27], v[70:71]
	v_pk_fma_f32 v[8:9], v[12:13], v[68:69], v[4:5]
	v_cvt_pk_bf16_f32 v3, v2, v3
	v_pk_fma_f32 v[10:11], v[10:11], v[66:67], v[6:7]
	v_pk_add_f32 v[94:95], v[8:9], v[96:97]
	v_cvt_pk_bf16_f32 v5, v4, v5
	v_cvt_pk_bf16_f32 v4, v6, v7
	ds_read_b128 v[6:9], v213 offset:14336
	v_pk_add_f32 v[96:97], v[10:11], v[98:99]
	ds_read_b128 v[10:13], v213 offset:15360
	v_cvt_pk_bf16_f32 v2, v30, v31
	s_waitcnt lgkmcnt(1)
	v_pk_mul_f32 v[30:31], v[6:7], v[66:67]
	v_mfma_f32_32x32x16_bf16 v[34:49], v[14:17], v[2:5], v[34:49]
	s_waitcnt lgkmcnt(0)
	v_mul_f32_e32 v10, v10, v70
	v_mul_f32_e32 v11, v11, v71
	v_mul_f32_e32 v2, v8, v68
	v_mul_f32_e32 v3, v9, v69
	v_pk_mul_f32 v[4:5], v[12:13], v[72:73]
	v_pk_fma_f32 v[6:7], v[6:7], v[66:67], v[10:11]
	v_pk_fma_f32 v[8:9], v[8:9], v[68:69], v[4:5]
	v_pk_add_f32 v[92:93], v[6:7], v[92:93]
	v_cvt_pk_bf16_f32 v3, v2, v3
	v_pk_add_f32 v[90:91], v[8:9], v[32:33]
	v_cvt_pk_bf16_f32 v5, v4, v5
	v_cvt_pk_bf16_f32 v4, v10, v11
	ds_read_b128 v[26:29], v213 offset:36864
	ds_read_b128 v[6:9], v213 offset:16384
	v_cvt_pk_bf16_f32 v2, v30, v31
	ds_read_b128 v[98:101], v213 offset:25600
	ds_read_b128 v[102:105], v213 offset:37888
	v_mfma_f32_32x32x16_bf16 v[50:65], v[14:17], v[2:5], v[50:65]
	ds_read_b128 v[2:5], v213 offset:17408
	ds_read_b128 v[30:33], v213 offset:24576
	s_waitcnt lgkmcnt(4)
	v_pk_mul_f32 v[12:13], v[6:7], v[18:19]
	v_pk_mul_f32 v[10:11], v[8:9], v[20:21]
	s_waitcnt lgkmcnt(1)
	v_pk_mul_f32 v[14:15], v[2:3], v[22:23]
	v_pk_mul_f32 v[22:23], v[98:99], v[22:23]
	v_pk_fma_f32 v[112:113], v[6:7], v[18:19], v[14:15]
	s_waitcnt lgkmcnt(0)
	v_pk_mul_f32 v[114:115], v[30:31], v[18:19]
	v_pk_fma_f32 v[118:119], v[30:31], v[18:19], v[22:23]
	v_pk_mul_f32 v[4:5], v[4:5], v[24:25]
	v_pk_mul_f32 v[106:107], v[32:33], v[20:21]
	v_pk_mul_f32 v[24:25], v[100:101], v[24:25]
	ds_read_b128 v[98:101], v213 offset:18432
	v_cvt_pk_bf16_f32 v19, v106, v107
	ds_read_b128 v[106:109], v213 offset:19456
	v_pk_fma_f32 v[110:111], v[8:9], v[20:21], v[4:5]
	v_cvt_pk_bf16_f32 v5, v4, v5
	v_cvt_pk_bf16_f32 v3, v10, v11
	v_cvt_pk_bf16_f32 v4, v14, v15
	s_waitcnt lgkmcnt(0)
	v_pk_mul_f32 v[106:107], v[106:107], v[86:87]
	v_cvt_pk_bf16_f32 v2, v12, v13
	v_pk_mul_f32 v[120:121], v[98:99], v[82:83]
	v_pk_mul_f32 v[108:109], v[108:109], v[88:89]
	v_pk_fma_f32 v[98:99], v[98:99], v[82:83], v[106:107]
	v_mfma_f32_32x32x16_bf16 v[2:17], v[26:29], v[2:5], 0
	v_cvt_pk_bf16_f32 v18, v114, v115
	v_mul_f32_e32 v114, v100, v84
	v_mul_f32_e32 v115, v101, v85
	v_fma_f32 v100, v100, v84, v108
	v_fma_f32 v101, v101, v85, v109
	v_pk_add_f32 v[124:125], v[98:99], v[112:113]
	v_pk_add_f32 v[122:123], v[100:101], v[110:111]
	v_cvt_pk_bf16_f32 v101, v108, v109
	v_cvt_pk_bf16_f32 v100, v106, v107
	ds_read_b128 v[106:109], v213 offset:26624
	v_pk_fma_f32 v[116:117], v[32:33], v[20:21], v[24:25]
	v_cvt_pk_bf16_f32 v21, v24, v25
	v_cvt_pk_bf16_f32 v20, v22, v23
	ds_read_b128 v[110:113], v213 offset:27648
	v_cvt_pk_bf16_f32 v99, v114, v115
	v_mfma_f32_32x32x16_bf16 v[18:33], v[26:29], v[18:21], 0
	v_cvt_pk_bf16_f32 v98, v120, v121
	s_waitcnt lgkmcnt(1)
	v_mul_f32_e32 v114, v106, v82
	v_mul_f32_e32 v115, v107, v83
	s_waitcnt lgkmcnt(0)
	v_pk_mul_f32 v[86:87], v[110:111], v[86:87]
	v_pk_mul_f32 v[88:89], v[112:113], v[88:89]
	v_pk_fma_f32 v[82:83], v[106:107], v[82:83], v[86:87]
	v_mfma_f32_32x32x16_bf16 v[2:17], v[102:105], v[98:101], v[2:17]
	v_mul_f32_e32 v98, v108, v84
	v_mul_f32_e32 v99, v109, v85
	v_fma_f32 v84, v108, v84, v88
	v_fma_f32 v85, v109, v85, v89
	v_add_f32_e32 v108, v82, v118
	v_add_f32_e32 v109, v83, v119
	v_cvt_pk_bf16_f32 v83, v98, v99
	v_pk_add_f32 v[106:107], v[84:85], v[116:117]
	v_cvt_pk_bf16_f32 v85, v88, v89
	v_cvt_pk_bf16_f32 v84, v86, v87
	ds_read_b128 v[86:89], v213 offset:38912
	ds_read_b128 v[98:101], v213 offset:20480
	v_cvt_pk_bf16_f32 v82, v114, v115
	s_waitcnt lgkmcnt(0)
	v_pk_mul_f32 v[110:111], v[100:101], v[76:77]
	v_mfma_f32_32x32x16_bf16 v[18:33], v[102:105], v[82:85], v[18:33]
	ds_read_b128 v[82:85], v213 offset:21504
	ds_read_b128 v[102:105], v213 offset:28672
	v_mul_f32_e32 v112, v98, v74
	v_mul_f32_e32 v113, v99, v75
	s_waitcnt lgkmcnt(1)
	v_pk_mul_f32 v[84:85], v[84:85], v[80:81]
	v_pk_mul_f32 v[114:115], v[82:83], v[78:79]
	v_pk_fma_f32 v[82:83], v[100:101], v[76:77], v[84:85]
	v_cvt_pk_bf16_f32 v85, v84, v85
	v_pk_add_f32 v[116:117], v[82:83], v[122:123]
	v_cvt_pk_bf16_f32 v83, v110, v111
	v_cvt_pk_bf16_f32 v84, v114, v115
	v_cvt_pk_bf16_f32 v82, v112, v113
	v_pk_fma_f32 v[98:99], v[98:99], v[74:75], v[114:115]
	s_waitcnt lgkmcnt(0)
	v_pk_mul_f32 v[112:113], v[102:103], v[74:75]
	v_mfma_f32_32x32x16_bf16 v[2:17], v[86:89], v[82:85], v[2:17]
	ds_read_b128 v[82:85], v213 offset:29696
	v_add_f32_e32 v118, v98, v124
	v_add_f32_e32 v119, v99, v125
	v_mul_f32_e32 v110, v104, v76
	v_mul_f32_e32 v111, v105, v77
	ds_read_b128 v[98:101], v213 offset:39936
	s_waitcnt lgkmcnt(1)
	v_pk_mul_f32 v[78:79], v[82:83], v[78:79]
	v_pk_mul_f32 v[80:81], v[84:85], v[80:81]
	v_pk_fma_f32 v[74:75], v[102:103], v[74:75], v[78:79]
	v_pk_fma_f32 v[76:77], v[104:105], v[76:77], v[80:81]
	v_pk_add_f32 v[104:105], v[74:75], v[108:109]
	v_pk_add_f32 v[102:103], v[76:77], v[106:107]
	v_cvt_pk_bf16_f32 v77, v80, v81
	v_cvt_pk_bf16_f32 v76, v78, v79
	ds_read_b128 v[78:81], v213 offset:22528
	ds_read_b128 v[82:85], v213 offset:23552
	v_cvt_pk_bf16_f32 v75, v110, v111
	v_cvt_pk_bf16_f32 v74, v112, v113
	s_waitcnt lgkmcnt(0)
	v_pk_mul_f32 v[82:83], v[82:83], v[70:71]
	v_mfma_f32_32x32x16_bf16 v[18:33], v[86:89], v[74:77], v[18:33]
	v_mul_f32_e32 v74, v80, v68
	v_mul_f32_e32 v75, v81, v69
	v_mul_f32_e32 v76, v84, v72
	v_mul_f32_e32 v77, v85, v73
	v_mul_f32_e32 v86, v78, v66
	v_mul_f32_e32 v87, v79, v67
	v_pk_fma_f32 v[80:81], v[80:81], v[68:69], v[76:77]
	v_pk_fma_f32 v[78:79], v[78:79], v[66:67], v[82:83]
	v_cvt_pk_bf16_f32 v75, v74, v75
	v_pk_add_f32 v[88:89], v[80:81], v[116:117]
	v_pk_add_f32 v[106:107], v[78:79], v[118:119]
	ds_read_b128 v[78:81], v213 offset:30720
	v_cvt_pk_bf16_f32 v77, v76, v77
	v_cvt_pk_bf16_f32 v76, v82, v83
	ds_read_b128 v[82:85], v213 offset:31744
	v_cvt_pk_bf16_f32 v74, v86, v87
	s_waitcnt lgkmcnt(0)
	v_pk_mul_f32 v[72:73], v[84:85], v[72:73]
	v_mfma_f32_32x32x16_bf16 v[2:17], v[98:101], v[74:77], v[2:17]
	v_mul_f32_e32 v74, v80, v68
	v_mul_f32_e32 v75, v81, v69
	v_fma_f32 v68, v80, v68, v72
	v_fma_f32 v69, v81, v69, v73
	v_mul_f32_e32 v70, v82, v70
	v_mul_f32_e32 v71, v83, v71
	v_pk_add_f32 v[84:85], v[68:69], v[102:103]
	v_cvt_pk_bf16_f32 v69, v72, v73
	v_add_f32_e32 v72, v97, v96
	v_add_f32_e32 v73, v94, v95
	v_pk_mul_f32 v[76:77], v[78:79], v[66:67]
	v_pk_fma_f32 v[66:67], v[78:79], v[66:67], v[70:71]
	v_add_f32_e32 v72, v72, v73
	v_pk_add_f32 v[86:87], v[66:67], v[104:105]
	v_mov_b32_e32 v66, v72
	s_nop 1
	v_permlane32_swap_b32_e32 v72, v66
	v_add_f32_e32 v66, v72, v66
	v_cvt_pk_bf16_f32 v67, v74, v75
	v_rcp_f32_e32 v74, v66
	v_cvt_pk_bf16_f32 v68, v70, v71
	v_cvt_pk_bf16_f32 v66, v76, v77
	v_pk_mul_f32 v[70:71], v[46:47], v[74:75] op_sel_hi:[1,0]
	s_nop 0
	v_mfma_f32_32x32x16_bf16 v[18:33], v[98:101], v[66:69], v[18:33]
	v_mul_f32_e32 v66, v42, v74
	v_mul_f32_e32 v67, v43, v74
	v_add_f32_e32 v42, v93, v92
	v_add_f32_e32 v43, v90, v91
	v_pk_mul_f32 v[68:69], v[44:45], v[74:75] op_sel_hi:[1,0]
	v_add_f32_e32 v42, v42, v43
	v_mov_b32_e32 v43, v42
	s_nop 1
	v_permlane32_swap_b32_e32 v42, v43
	v_add_f32_e32 v42, v42, v43
	v_rcp_f32_e32 v42, v42
	v_add_f32_e32 v44, v107, v106
	v_add_f32_e32 v45, v88, v89
	v_pk_mul_f32 v[72:73], v[48:49], v[74:75] op_sel_hi:[1,0]
	v_add_f32_e32 v44, v44, v45
	v_pk_mul_f32 v[36:37], v[36:37], v[74:75] op_sel_hi:[1,0]
	v_pk_mul_f32 v[38:39], v[38:39], v[74:75] op_sel_hi:[1,0]
	v_pk_mul_f32 v[40:41], v[40:41], v[74:75] op_sel_hi:[1,0]
	v_pk_mul_f32 v[34:35], v[34:35], v[74:75] op_sel_hi:[1,0]
	v_pk_mul_f32 v[74:75], v[58:59], v[42:43] op_sel_hi:[1,0]
	v_pk_mul_f32 v[78:79], v[60:61], v[42:43] op_sel_hi:[1,0]
	v_pk_mul_f32 v[80:81], v[62:63], v[42:43] op_sel_hi:[1,0]
	v_pk_mul_f32 v[82:83], v[64:65], v[42:43] op_sel_hi:[1,0]
	v_pk_mul_f32 v[92:93], v[52:53], v[42:43] op_sel_hi:[1,0]
	v_mov_b32_e32 v43, v44
	s_nop 1
	v_permlane32_swap_b32_e32 v44, v43
	v_add_f32_e32 v43, v44, v43
	v_rcp_f32_e32 v76, v43
	v_pk_mul_f32 v[96:97], v[54:55], v[42:43] op_sel_hi:[1,0]
	v_pk_mul_f32 v[94:95], v[56:57], v[42:43] op_sel_hi:[1,0]
	v_pk_mul_f32 v[98:99], v[50:51], v[42:43] op_sel_hi:[1,0]
	v_pk_mul_f32 v[100:101], v[4:5], v[76:77] op_sel_hi:[1,0]
	v_pk_mov_b32 v[4:5], v[86:87], v[84:85] op_sel:[1,0]
	v_mov_b32_e32 v87, v85
	v_pk_add_f32 v[4:5], v[4:5], v[86:87]
	v_pk_mul_f32 v[102:103], v[6:7], v[76:77] op_sel_hi:[1,0]
	v_pk_add_f32 v[104:105], v[4:5], v[4:5] op_sel:[0,1] op_sel_hi:[1,0]
	v_cvt_pk_bf16_f32 v7, v40, v41
	ds_read_b128 v[84:87], v150 offset:52224
	ds_read_b128 v[50:53], v150 offset:35840
	ds_read_b128 v[54:57], v150 offset:36864
	ds_read_b128 v[58:61], v150 offset:37888
	ds_read_b128 v[62:65], v150 offset:38912
	v_cvt_pk_bf16_f32 v6, v38, v39
	v_cvt_pk_bf16_f32 v5, v36, v37
	v_cvt_pk_bf16_f32 v4, v34, v35
	ds_read_b128 v[88:91], v150 offset:53248
	ds_read_b128 v[34:37], v150 offset:39936
	ds_read_b128 v[38:41], v150 offset:40960
	ds_read_b128 v[42:45], v150 offset:41984
	ds_read_b128 v[46:49], v150 offset:43008
	v_cvt_pk_bf16_f32 v95, v94, v95
	v_cvt_pk_bf16_f32 v94, v96, v97
	v_cvt_pk_bf16_f32 v93, v92, v93
	v_cvt_pk_bf16_f32 v92, v98, v99
	s_waitcnt lgkmcnt(5)
	v_mfma_f32_32x32x16_bf16 v[50:65], v[84:87], v[4:7], v[50:65]
	v_mul_f32_e32 v10, v10, v76
	v_mul_f32_e32 v11, v11, v76
	v_mul_f32_e32 v12, v12, v76
	v_mul_f32_e32 v13, v13, v76
	v_mul_f32_e32 v8, v8, v76
	v_mul_f32_e32 v9, v9, v76
	v_mov_b32_e32 v77, v104
	s_nop 1
	v_permlane32_swap_b32_e32 v104, v77
	v_cvt_pk_bf16_f32 v73, v72, v73
	s_waitcnt lgkmcnt(0)
	v_mfma_f32_32x32x16_bf16 v[34:49], v[84:87], v[92:95], v[34:49]
	v_cvt_pk_bf16_f32 v72, v70, v71
	v_cvt_pk_bf16_f32 v70, v66, v67
	v_add_f32_e32 v66, v104, v77
	v_cvt_pk_bf16_f32 v71, v68, v69
	v_rcp_f32_e32 v104, v66
	v_cvt_pk_bf16_f32 v69, v82, v83
	v_cvt_pk_bf16_f32 v68, v80, v81
	v_cvt_pk_bf16_f32 v67, v78, v79
	v_cvt_pk_bf16_f32 v66, v74, v75
	ds_read_b128 v[78:81], v150 offset:54272
	v_mfma_f32_32x32x16_bf16 v[50:65], v[88:91], v[70:73], v[50:65]
	v_mul_f32_e32 v2, v2, v76
	v_mul_f32_e32 v3, v3, v76
	v_mul_f32_e32 v20, v20, v104
	v_mul_f32_e32 v21, v21, v104
	v_cvt_pk_bf16_f32 v85, v8, v9
	v_cvt_pk_bf16_f32 v82, v2, v3
	v_pk_mul_f32 v[2:3], v[22:23], v[104:105] op_sel_hi:[1,0]
	v_pk_mul_f32 v[8:9], v[24:25], v[104:105] op_sel_hi:[1,0]
	v_pk_mul_f32 v[18:19], v[18:19], v[104:105] op_sel_hi:[1,0]
	v_mfma_f32_32x32x16_bf16 v[34:49], v[88:91], v[66:69], v[34:49]
	v_cvt_pk_bf16_f32 v84, v102, v103
	v_cvt_pk_bf16_f32 v83, v100, v101
	ds_read_b128 v[86:89], v150 offset:55296
	v_cvt_pk_bf16_f32 v99, v8, v9
	v_cvt_pk_bf16_f32 v98, v2, v3
	v_cvt_pk_bf16_f32 v97, v20, v21
	v_cvt_pk_bf16_f32 v96, v18, v19
	s_waitcnt lgkmcnt(1)
	v_mfma_f32_32x32x16_bf16 v[50:65], v[78:81], v[82:85], v[50:65]
	v_mul_f32_e32 v2, v14, v76
	v_mul_f32_e32 v3, v15, v76
	v_mul_f32_e32 v8, v16, v76
	v_mul_f32_e32 v9, v17, v76
	v_mul_f32_e32 v14, v26, v104
	v_mul_f32_e32 v15, v27, v104
	v_cvt_pk_bf16_f32 v77, v8, v9
	v_cvt_pk_bf16_f32 v76, v2, v3
	v_cvt_pk_bf16_f32 v74, v10, v11
	v_pk_mul_f32 v[2:3], v[28:29], v[104:105] op_sel_hi:[1,0]
	v_mfma_f32_32x32x16_bf16 v[34:49], v[78:81], v[96:99], v[34:49]
	v_mul_f32_e32 v8, v30, v104
	v_mul_f32_e32 v9, v31, v104
	v_mul_f32_e32 v10, v32, v104
	v_mul_f32_e32 v11, v33, v104
	v_cvt_pk_bf16_f32 v75, v12, v13
	v_cvt_pk_bf16_f32 v81, v10, v11
	v_cvt_pk_bf16_f32 v80, v8, v9
	v_cvt_pk_bf16_f32 v79, v2, v3
	v_cvt_pk_bf16_f32 v78, v14, v15
	s_waitcnt lgkmcnt(0)
	v_mfma_f32_32x32x16_bf16 v[50:65], v[86:89], v[74:77], v[50:65]
	v_mfma_f32_32x32x16_bf16 v[34:49], v[86:89], v[78:81], v[34:49]
	ds_read_b128 v[86:89], v150 offset:56320
	ds_read_b128 v[18:21], v150 offset:44032
	ds_read_b128 v[22:25], v150 offset:45056
	ds_read_b128 v[26:29], v150 offset:46080
	ds_read_b128 v[30:33], v150 offset:47104
	ds_read_b128 v[100:103], v150 offset:57344
	s_waitcnt lgkmcnt(1)
	v_mfma_f32_32x32x16_bf16 v[18:33], v[86:89], v[4:7], v[18:33]
	ds_read_b128 v[2:5], v150 offset:48128
	ds_read_b128 v[6:9], v150 offset:49152
	ds_read_b128 v[10:13], v150 offset:50176
	ds_read_b128 v[14:17], v150 offset:51200
	s_waitcnt lgkmcnt(0)
	v_mfma_f32_32x32x16_bf16 v[2:17], v[86:89], v[92:95], v[2:17]
	v_mfma_f32_32x32x16_bf16 v[18:33], v[100:103], v[70:73], v[18:33]
	v_mfma_f32_32x32x16_bf16 v[2:17], v[100:103], v[66:69], v[2:17]
	ds_read_b128 v[66:69], v150 offset:58368
	ds_read_b128 v[70:73], v150 offset:59392
	s_waitcnt lgkmcnt(1)
	v_mfma_f32_32x32x16_bf16 v[18:33], v[66:69], v[82:85], v[18:33]
	v_mfma_f32_32x32x16_bf16 v[2:17], v[66:69], v[96:99], v[2:17]
	s_waitcnt lgkmcnt(0)
	v_mfma_f32_32x32x16_bf16 v[18:33], v[70:73], v[74:77], v[18:33]
	v_mfma_f32_32x32x16_bf16 v[2:17], v[70:73], v[78:81], v[2:17]
	s_nop 10
	v_mul_f32_e32 v66, v22, v22
	v_mul_f32_e32 v67, v23, v23
	v_mul_f32_e32 v68, v30, v30
	v_mul_f32_e32 v69, v31, v31
	v_mul_f32_e32 v70, v24, v24
	v_mul_f32_e32 v71, v25, v25
	v_pk_mul_f32 v[72:73], v[32:33], v[32:33]
	v_pk_mul_f32 v[74:75], v[20:21], v[20:21]
	v_pk_mul_f32 v[76:77], v[28:29], v[28:29]
	v_pk_mul_f32 v[78:79], v[26:27], v[26:27]
	v_pk_mul_f32 v[80:81], v[18:19], v[18:19]
	v_pk_fma_f32 v[78:79], v[58:59], v[58:59], v[78:79]
	v_pk_fma_f32 v[76:77], v[60:61], v[60:61], v[76:77]
	v_pk_fma_f32 v[74:75], v[52:53], v[52:53], v[74:75]
	v_pk_fma_f32 v[72:73], v[64:65], v[64:65], v[72:73]
	v_pk_fma_f32 v[70:71], v[56:57], v[56:57], v[70:71]
	v_pk_fma_f32 v[68:69], v[62:63], v[62:63], v[68:69]
	v_pk_fma_f32 v[66:67], v[54:55], v[54:55], v[66:67]
	v_pk_fma_f32 v[80:81], v[50:51], v[50:51], v[80:81]
	v_pk_add_f32 v[66:67], v[66:67], v[68:69]
	v_pk_add_f32 v[68:69], v[70:71], v[72:73]
	v_pk_add_f32 v[70:71], v[74:75], v[76:77]
	v_pk_add_f32 v[72:73], v[80:81], v[78:79]
	v_pk_add_f32 v[68:69], v[70:71], v[68:69]
	v_pk_add_f32 v[66:67], v[72:73], v[66:67]
	v_pk_mul_f32 v[72:73], v[14:15], v[14:15]
	v_pk_mov_b32 v[70:71], v[66:67], v[68:69] op_sel:[1,0]
	v_mov_b32_e32 v67, v69
	v_pk_add_f32 v[66:67], v[70:71], v[66:67]
	v_pk_mul_f32 v[70:71], v[6:7], v[6:7]
	v_pk_mul_f32 v[74:75], v[8:9], v[8:9]
	v_pk_mul_f32 v[76:77], v[16:17], v[16:17]
	v_pk_mul_f32 v[78:79], v[4:5], v[4:5]
	v_pk_mul_f32 v[80:81], v[12:13], v[12:13]
	v_pk_mul_f32 v[82:83], v[10:11], v[10:11]
	v_pk_mul_f32 v[84:85], v[2:3], v[2:3]
	v_pk_fma_f32 v[82:83], v[42:43], v[42:43], v[82:83]
	v_pk_fma_f32 v[80:81], v[44:45], v[44:45], v[80:81]
	v_pk_fma_f32 v[78:79], v[36:37], v[36:37], v[78:79]
	v_pk_fma_f32 v[76:77], v[48:49], v[48:49], v[76:77]
	v_pk_fma_f32 v[74:75], v[40:41], v[40:41], v[74:75]
	v_pk_fma_f32 v[72:73], v[46:47], v[46:47], v[72:73]
	v_pk_fma_f32 v[70:71], v[38:39], v[38:39], v[70:71]
	v_pk_fma_f32 v[84:85], v[34:35], v[34:35], v[84:85]
	v_pk_add_f32 v[70:71], v[70:71], v[72:73]
	v_pk_add_f32 v[72:73], v[74:75], v[76:77]
	v_pk_add_f32 v[74:75], v[78:79], v[80:81]
	v_pk_add_f32 v[76:77], v[84:85], v[82:83]
	v_pk_add_f32 v[72:73], v[74:75], v[72:73]
	v_pk_add_f32 v[70:71], v[76:77], v[70:71]
	v_pk_add_f32 v[66:67], v[66:67], v[66:67] op_sel:[0,1] op_sel_hi:[1,0]
	v_add_f32_e32 v70, v71, v70
	v_add_f32_e32 v71, v72, v73
	v_mov_b32_e32 v69, v66
	v_add_f32_e32 v70, v70, v71
	s_nop 0
	v_permlane32_swap_b32_e32 v66, v69
	v_mov_b32_e32 v68, v70
	s_nop 1
	v_permlane32_swap_b32_e32 v70, v68
	v_mov_b32_e32 v71, v66
	v_pk_add_f32 v[66:67], v[70:71], v[68:69]
	v_pk_fma_f32 v[66:67], v[66:67], s[0:1], v[152:153] op_sel_hi:[1,0,0]
	s_mov_b32 s1, 0x800000
	v_rsq_f32_e32 v68, v67
	s_nop 0
	v_pk_mul_f32 v[158:159], v[50:51], v[68:69] op_sel_hi:[1,0]
	v_pk_mul_f32 v[50:51], v[18:19], v[68:69] op_sel_hi:[1,0]
	v_pk_mul_f32 v[80:81], v[60:61], v[68:69] op_sel_hi:[1,0]
	v_pk_mul_f32 v[60:61], v[28:29], v[68:69] op_sel_hi:[1,0]
	v_pk_mul_f32 v[78:79], v[58:59], v[68:69] op_sel_hi:[1,0]
	v_pk_mul_f32 v[160:161], v[52:53], v[68:69] op_sel_hi:[1,0]
	v_pk_mul_f32 v[82:83], v[54:55], v[68:69] op_sel_hi:[1,0]
	v_rsq_f32_e32 v28, v66
	v_pk_mul_f32 v[168:169], v[56:57], v[68:69] op_sel_hi:[1,0]
	v_pk_mul_f32 v[58:59], v[26:27], v[68:69] op_sel_hi:[1,0]
	v_pk_mul_f32 v[52:53], v[20:21], v[68:69] op_sel_hi:[1,0]
	v_pk_mul_f32 v[54:55], v[22:23], v[68:69] op_sel_hi:[1,0]
	v_pk_mul_f32 v[56:57], v[24:25], v[68:69] op_sel_hi:[1,0]
	v_pk_mul_f32 v[18:19], v[42:43], v[28:29] op_sel_hi:[1,0]
	v_pk_mul_f32 v[20:21], v[44:45], v[28:29] op_sel_hi:[1,0]
	v_pk_mul_f32 v[22:23], v[46:47], v[28:29] op_sel_hi:[1,0]
	v_pk_mul_f32 v[26:27], v[48:49], v[28:29] op_sel_hi:[1,0]
	v_pk_mul_f32 v[162:163], v[34:35], v[28:29] op_sel_hi:[1,0]
	v_pk_mul_f32 v[164:165], v[36:37], v[28:29] op_sel_hi:[1,0]
	v_pk_mul_f32 v[166:167], v[38:39], v[28:29] op_sel_hi:[1,0]
	v_pk_mul_f32 v[24:25], v[40:41], v[28:29] op_sel_hi:[1,0]
	v_pk_mul_f32 v[104:105], v[2:3], v[28:29] op_sel_hi:[1,0]
	v_pk_mul_f32 v[112:113], v[4:5], v[28:29] op_sel_hi:[1,0]
	ds_read_b128 v[2:5], v150 offset:60416
	ds_read_b128 v[34:37], v174 offset:32768
	ds_read_b128 v[38:41], v174 offset:32800
	ds_read_b128 v[42:45], v174 offset:32832
	ds_read_b128 v[46:49], v174 offset:32864
	v_cvt_pk_bf16_f32 v129, v168, v169
	v_cvt_pk_bf16_f32 v128, v82, v83
	v_cvt_pk_bf16_f32 v127, v160, v161
	v_cvt_pk_bf16_f32 v126, v158, v159
	v_cvt_pk_bf16_f32 v137, v24, v25
	v_cvt_pk_bf16_f32 v136, v166, v167
	v_cvt_pk_bf16_f32 v135, v164, v165
	s_waitcnt lgkmcnt(0)
	v_mfma_f32_32x32x16_bf16 v[86:101], v[2:5], v[126:129], v[34:49]
	v_cvt_pk_bf16_f32 v134, v162, v163
	v_mul_f32_e32 v84, v62, v68
	v_mul_f32_e32 v85, v63, v68
	v_mul_f32_e32 v170, v64, v68
	v_mul_f32_e32 v171, v65, v68
	v_pk_mul_f32 v[62:63], v[30:31], v[68:69] op_sel_hi:[1,0]
	v_pk_mul_f32 v[64:65], v[32:33], v[68:69] op_sel_hi:[1,0]
	v_pk_mul_f32 v[116:117], v[6:7], v[28:29] op_sel_hi:[1,0]
	v_pk_mul_f32 v[154:155], v[8:9], v[28:29] op_sel_hi:[1,0]
	v_mfma_f32_32x32x16_bf16 v[34:49], v[2:5], v[134:137], v[34:49]
	ds_read_b128 v[6:9], v150 offset:61440
	ds_read_b128 v[66:69], v174 offset:32896
	ds_read_b128 v[106:109], v150 offset:64512
	v_cvt_pk_bf16_f32 v125, v170, v171
	v_cvt_pk_bf16_f32 v124, v84, v85
	v_cvt_pk_bf16_f32 v123, v80, v81
	v_cvt_pk_bf16_f32 v122, v78, v79
	v_cvt_pk_bf16_f32 v149, v26, v27
	v_cvt_pk_bf16_f32 v148, v22, v23
	v_cvt_pk_bf16_f32 v147, v20, v21
	v_cvt_pk_bf16_f32 v146, v18, v19
	s_waitcnt lgkmcnt(2)
	v_mfma_f32_32x32x16_bf16 v[86:101], v[6:9], v[122:125], v[86:101]
	v_mul_f32_e32 v102, v10, v28
	v_mul_f32_e32 v103, v11, v28
	v_mul_f32_e32 v110, v12, v28
	v_mul_f32_e32 v111, v13, v28
	v_mul_f32_e32 v114, v14, v28
	v_mul_f32_e32 v115, v15, v28
	v_pk_mul_f32 v[156:157], v[16:17], v[28:29] op_sel_hi:[1,0]
	ds_read_b128 v[176:179], v174 offset:33536
	ds_read_b128 v[180:183], v174 offset:33568
	ds_read_b128 v[184:187], v174 offset:33600
	ds_read_b128 v[28:31], v174 offset:33632
	ds_read_b128 v[188:191], v174 offset:33792
	ds_read_b128 v[192:195], v174 offset:33824
	ds_read_b128 v[196:199], v174 offset:33856
	ds_read_b128 v[200:203], v174 offset:33888
	ds_read_b128 v[204:207], v150 offset:62464
	v_cvt_pk_bf16_f32 v133, v56, v57
	v_mfma_f32_32x32x16_bf16 v[34:49], v[6:9], v[146:149], v[34:49]
	v_cvt_pk_bf16_f32 v132, v54, v55
	v_cvt_pk_bf16_f32 v131, v52, v53
	v_cvt_pk_bf16_f32 v130, v50, v51
	ds_read_b128 v[70:73], v174 offset:33664
	ds_read_b128 v[74:77], v174 offset:33920
	ds_read_b128 v[208:211], v150 offset:63488
	v_cvt_pk_bf16_f32 v145, v154, v155
	v_cvt_pk_bf16_f32 v144, v116, v117
	v_cvt_pk_bf16_f32 v143, v112, v113
	v_cvt_pk_bf16_f32 v142, v104, v105
	s_waitcnt lgkmcnt(3)
	v_mfma_f32_32x32x16_bf16 v[86:101], v[204:207], v[130:133], v[86:101]
	v_cvt_pk_bf16_f32 v121, v64, v65
	v_cvt_pk_bf16_f32 v120, v62, v63
	v_cvt_pk_bf16_f32 v119, v60, v61
	v_cvt_pk_bf16_f32 v118, v58, v59
	v_cvt_pk_bf16_f32 v141, v156, v157
	v_cvt_pk_bf16_f32 v140, v114, v115
	v_cvt_pk_bf16_f32 v139, v110, v111
	v_mfma_f32_32x32x16_bf16 v[34:49], v[204:207], v[142:145], v[34:49]
	v_cvt_pk_bf16_f32 v138, v102, v103
	v_fma_f32 v16, v30, v170, v202
	v_fma_f32 v17, v31, v171, v203
	v_fma_f32 v14, v28, v84, v200
	v_fma_f32 v15, v29, v85, v201
	v_pk_fma_f32 v[12:13], v[186:187], v[80:81], v[198:199]
	v_pk_fma_f32 v[10:11], v[184:185], v[78:79], v[196:197]
	v_pk_fma_f32 v[8:9], v[182:183], v[168:169], v[194:195]
	s_waitcnt lgkmcnt(0)
	v_mfma_f32_32x32x16_bf16 v[86:101], v[208:211], v[118:121], v[86:101]
	v_fma_f32 v6, v180, v82, v192
	v_fma_f32 v7, v181, v83, v193
	ds_read_b128 v[78:81], v174 offset:33760
	ds_read_b128 v[82:85], v174 offset:33248
	v_fma_f32 v4, v178, v160, v190
	v_fma_f32 v5, v179, v161, v191
	v_pk_fma_f32 v[2:3], v[176:177], v[158:159], v[188:189]
	v_pk_fma_f32 v[32:33], v[30:31], v[26:27], v[202:203]
	v_pk_fma_f32 v[30:31], v[28:29], v[22:23], v[200:201]
	v_pk_fma_f32 v[28:29], v[186:187], v[20:21], v[198:199]
	v_pk_fma_f32 v[26:27], v[184:185], v[18:19], v[196:197]
	v_pk_fma_f32 v[24:25], v[182:183], v[24:25], v[194:195]
	v_pk_fma_f32 v[22:23], v[180:181], v[166:167], v[192:193]
	v_pk_fma_f32 v[20:21], v[178:179], v[164:165], v[190:191]
	v_pk_fma_f32 v[18:19], v[176:177], v[162:163], v[188:189]
	ds_read_b128 v[158:161], v174 offset:33696
	ds_read_b128 v[162:165], v174 offset:33728
	ds_read_b128 v[166:169], v174 offset:33952
	ds_read_b128 v[176:179], v174 offset:33984
	ds_read_b128 v[180:183], v174 offset:34016
	ds_read_b128 v[184:187], v212 offset:11264
	v_mfma_f32_32x32x16_bf16 v[34:49], v[208:211], v[138:141], v[34:49]
	v_cvt_pk_bf16_f32 v86, v86, v87
	v_cvt_pk_bf16_f32 v87, v88, v89
	v_cvt_pk_bf16_f32 v88, v90, v91
	v_cvt_pk_bf16_f32 v89, v92, v93
	ds_read_b128 v[90:93], v212 offset:12288
	v_pk_max_i16 v86, v86, 0
	v_pk_max_i16 v87, v87, 0
	v_pk_max_i16 v88, v88, 0
	v_pk_max_i16 v89, v89, 0
	s_nop 1
	s_nop 0
	v_cvt_pk_bf16_f32 v188, v34, v35
	v_cvt_pk_bf16_f32 v189, v36, v37
	v_cvt_pk_bf16_f32 v190, v38, v39
	v_cvt_pk_bf16_f32 v191, v40, v41
	s_waitcnt lgkmcnt(1)
	v_mfma_f32_32x32x16_bf16 v[2:17], v[184:187], v[86:89], v[2:17]
	v_pk_max_i16 v188, v188, 0
	v_pk_max_i16 v189, v189, 0
	v_pk_max_i16 v190, v190, 0
	v_pk_max_i16 v191, v191, 0
	v_cvt_pk_bf16_f32 v94, v94, v95
	v_cvt_pk_bf16_f32 v95, v96, v97
	v_cvt_pk_bf16_f32 v96, v98, v99
	v_cvt_pk_bf16_f32 v97, v100, v101
	v_cvt_pk_bf16_f32 v98, v42, v43
	v_cvt_pk_bf16_f32 v99, v44, v45
	v_mfma_f32_32x32x16_bf16 v[18:33], v[184:187], v[188:191], v[18:33]
	ds_read_b128 v[184:187], v212 offset:19456
	v_cvt_pk_bf16_f32 v100, v46, v47
	v_cvt_pk_bf16_f32 v101, v48, v49
	v_fma_f32 v64, v80, v64, v182
	v_fma_f32 v65, v81, v65, v183
	v_pk_fma_f32 v[62:63], v[78:79], v[62:63], v[180:181]
	v_pk_fma_f32 v[60:61], v[164:165], v[60:61], v[178:179]
	v_pk_fma_f32 v[58:59], v[162:163], v[58:59], v[176:177]
	v_pk_max_i16 v94, v94, 0
	v_pk_max_i16 v95, v95, 0
	v_pk_max_i16 v96, v96, 0
	v_pk_max_i16 v97, v97, 0
	v_pk_max_i16 v98, v98, 0
	v_pk_max_i16 v99, v99, 0
	v_pk_max_i16 v100, v100, 0
	v_pk_max_i16 v101, v101, 0
	v_pk_fma_f32 v[56:57], v[160:161], v[56:57], v[168:169]
	s_waitcnt lgkmcnt(1)
	v_mfma_f32_32x32x16_bf16 v[2:17], v[90:93], v[94:97], v[2:17]
	v_fma_f32 v54, v158, v54, v166
	v_fma_f32 v55, v159, v55, v167
	v_fma_f32 v52, v72, v52, v76
	v_fma_f32 v53, v73, v53, v77
	v_fma_f32 v50, v70, v50, v74
	v_fma_f32 v51, v71, v51, v75
	v_pk_fma_f32 v[48:49], v[80:81], v[156:157], v[182:183]
	v_pk_fma_f32 v[46:47], v[78:79], v[114:115], v[180:181]
	v_pk_fma_f32 v[44:45], v[164:165], v[110:111], v[178:179]
	v_pk_fma_f32 v[42:43], v[162:163], v[102:103], v[176:177]
	v_mfma_f32_32x32x16_bf16 v[18:33], v[90:93], v[98:101], v[18:33]
	ds_read_b128 v[90:93], v212 offset:20480
	v_fma_f32 v40, v160, v154, v168
	v_fma_f32 v41, v161, v155, v169
	v_fma_f32 v38, v158, v116, v166
	v_fma_f32 v39, v159, v117, v167
	v_pk_fma_f32 v[36:37], v[72:73], v[112:113], v[76:77]
	v_pk_fma_f32 v[34:35], v[70:71], v[104:105], v[74:75]
	s_waitcnt lgkmcnt(1)
	v_mfma_f32_32x32x16_bf16 v[50:65], v[184:187], v[86:89], v[50:65]
	ds_read_b128 v[70:73], v174 offset:32928
	ds_read_b128 v[74:77], v174 offset:32960
	ds_read_b128 v[78:81], v174 offset:32992
	ds_read_b128 v[86:89], v174 offset:33024
	ds_read_b128 v[110:113], v212 offset:1024
	v_mfma_f32_32x32x16_bf16 v[34:49], v[184:187], v[188:191], v[34:49]
	s_waitcnt lgkmcnt(5)
	v_mfma_f32_32x32x16_bf16 v[50:65], v[90:93], v[94:97], v[50:65]
	v_mfma_f32_32x32x16_bf16 v[34:49], v[90:93], v[98:101], v[34:49]
	s_waitcnt lgkmcnt(2)
	v_mfma_f32_32x32x16_bf16 v[90:105], v[106:109], v[126:129], v[66:81]
	v_mfma_f32_32x32x16_bf16 v[66:81], v[106:109], v[134:137], v[66:81]
	ds_read_b128 v[106:109], v212 offset:0
	s_waitcnt lgkmcnt(0)
	v_mfma_f32_32x32x16_bf16 v[90:105], v[106:109], v[122:125], v[90:105]
	v_mfma_f32_32x32x16_bf16 v[66:81], v[106:109], v[146:149], v[66:81]
	ds_read_b128 v[106:109], v212 offset:2048
	v_mfma_f32_32x32x16_bf16 v[90:105], v[110:113], v[130:133], v[90:105]
	v_mfma_f32_32x32x16_bf16 v[66:81], v[110:113], v[142:145], v[66:81]
	ds_read_b128 v[110:113], v212 offset:13312
	s_waitcnt lgkmcnt(1)
	v_mfma_f32_32x32x16_bf16 v[90:105], v[106:109], v[118:121], v[90:105]
	v_mfma_f32_32x32x16_bf16 v[66:81], v[106:109], v[138:141], v[66:81]
	s_nop 10
	v_cvt_pk_bf16_f32 v90, v90, v91
	v_cvt_pk_bf16_f32 v91, v92, v93
	v_cvt_pk_bf16_f32 v92, v94, v95
	v_cvt_pk_bf16_f32 v94, v98, v99
	v_cvt_pk_bf16_f32 v95, v100, v101
	ds_read_b128 v[98:101], v212 offset:21504
	v_cvt_pk_bf16_f32 v66, v66, v67
	v_cvt_pk_bf16_f32 v67, v68, v69
	v_cvt_pk_bf16_f32 v68, v70, v71
	v_cvt_pk_bf16_f32 v93, v96, v97
	v_cvt_pk_bf16_f32 v69, v72, v73
	ds_read_b128 v[70:73], v212 offset:14336
	v_pk_max_i16 v90, v90, 0
	v_pk_max_i16 v91, v91, 0
	v_pk_max_i16 v92, v92, 0
	v_pk_max_i16 v93, v93, 0
	v_pk_max_i16 v66, v66, 0
	v_pk_max_i16 v67, v67, 0
	v_pk_max_i16 v68, v68, 0
	v_pk_max_i16 v69, v69, 0
	v_cvt_pk_bf16_f32 v96, v102, v103
	s_waitcnt lgkmcnt(2)
	v_mfma_f32_32x32x16_bf16 v[2:17], v[110:113], v[90:93], v[2:17]
	v_cvt_pk_bf16_f32 v97, v104, v105
	v_cvt_pk_bf16_f32 v74, v74, v75
	v_cvt_pk_bf16_f32 v75, v76, v77
	v_cvt_pk_bf16_f32 v76, v78, v79
	v_cvt_pk_bf16_f32 v77, v80, v81
	v_pk_max_i16 v94, v94, 0
	v_pk_max_i16 v95, v95, 0
	v_pk_max_i16 v96, v96, 0
	v_pk_max_i16 v97, v97, 0
	v_pk_max_i16 v74, v74, 0
	v_pk_max_i16 v75, v75, 0
	v_pk_max_i16 v76, v76, 0
	v_pk_max_i16 v77, v77, 0
	v_mfma_f32_32x32x16_bf16 v[18:33], v[110:113], v[66:69], v[18:33]
	s_waitcnt lgkmcnt(1)
	v_mfma_f32_32x32x16_bf16 v[34:49], v[98:101], v[66:69], v[34:49]
	ds_read_b128 v[66:69], v212 offset:22528
	v_mfma_f32_32x32x16_bf16 v[50:65], v[98:101], v[90:93], v[50:65]
	s_waitcnt lgkmcnt(1)
	v_mfma_f32_32x32x16_bf16 v[2:17], v[70:73], v[94:97], v[2:17]
	v_mfma_f32_32x32x16_bf16 v[18:33], v[70:73], v[74:77], v[18:33]
	ds_read_b128 v[78:81], v212 offset:3072
	s_waitcnt lgkmcnt(1)
	v_mfma_f32_32x32x16_bf16 v[50:65], v[66:69], v[94:97], v[50:65]
	ds_read_b128 v[90:93], v174 offset:33056
	ds_read_b128 v[94:97], v174 offset:33088
	ds_read_b128 v[98:101], v174 offset:33120
	ds_read_b128 v[70:73], v174 offset:33152
	v_mfma_f32_32x32x16_bf16 v[34:49], v[66:69], v[74:77], v[34:49]
	ds_read_b128 v[66:69], v212 offset:4096
	ds_read_b128 v[74:77], v212 offset:5120
	s_waitcnt lgkmcnt(3)
	v_mfma_f32_32x32x16_bf16 v[102:117], v[78:81], v[126:129], v[86:101]
	v_mfma_f32_32x32x16_bf16 v[86:101], v[78:81], v[134:137], v[86:101]
	s_waitcnt lgkmcnt(1)
	v_mfma_f32_32x32x16_bf16 v[86:101], v[66:69], v[146:149], v[86:101]
	v_mfma_f32_32x32x16_bf16 v[102:117], v[66:69], v[122:125], v[102:117]
	ds_read_b128 v[66:69], v212 offset:6144
	s_waitcnt lgkmcnt(1)
	v_mfma_f32_32x32x16_bf16 v[86:101], v[74:77], v[142:145], v[86:101]
	v_mfma_f32_32x32x16_bf16 v[102:117], v[74:77], v[130:133], v[102:117]
	ds_read_b128 v[74:77], v212 offset:15360
	s_waitcnt lgkmcnt(1)
	v_mfma_f32_32x32x16_bf16 v[86:101], v[66:69], v[138:141], v[86:101]
	v_mfma_f32_32x32x16_bf16 v[102:117], v[66:69], v[118:121], v[102:117]
	s_nop 10
	v_cvt_pk_bf16_f32 v78, v86, v87
	v_cvt_pk_bf16_f32 v80, v90, v91
	v_cvt_pk_bf16_f32 v79, v88, v89
	v_cvt_pk_bf16_f32 v81, v92, v93
	ds_read_b128 v[86:89], v212 offset:16384
	ds_read_b128 v[90:93], v212 offset:23552
	v_cvt_pk_bf16_f32 v66, v102, v103
	v_cvt_pk_bf16_f32 v67, v104, v105
	v_cvt_pk_bf16_f32 v68, v106, v107
	v_cvt_pk_bf16_f32 v69, v108, v109
	v_pk_max_i16 v66, v66, 0
	v_pk_max_i16 v67, v67, 0
	v_pk_max_i16 v68, v68, 0
	v_pk_max_i16 v69, v69, 0
	v_pk_max_i16 v78, v78, 0
	v_pk_max_i16 v79, v79, 0
	v_pk_max_i16 v80, v80, 0
	v_pk_max_i16 v81, v81, 0
	v_cvt_pk_bf16_f32 v94, v94, v95
	s_waitcnt lgkmcnt(2)
	v_mfma_f32_32x32x16_bf16 v[18:33], v[74:77], v[78:81], v[18:33]
	v_cvt_pk_bf16_f32 v95, v96, v97
	v_cvt_pk_bf16_f32 v96, v98, v99
	v_cvt_pk_bf16_f32 v97, v100, v101
	v_pk_max_i16 v94, v94, 0
	v_pk_max_i16 v95, v95, 0
	v_pk_max_i16 v96, v96, 0
	v_pk_max_i16 v97, v97, 0
	v_mfma_f32_32x32x16_bf16 v[2:17], v[74:77], v[66:69], v[2:17]
	v_cvt_pk_bf16_f32 v74, v110, v111
	v_cvt_pk_bf16_f32 v75, v112, v113
	v_cvt_pk_bf16_f32 v76, v114, v115
	v_cvt_pk_bf16_f32 v77, v116, v117
	v_pk_max_i16 v74, v74, 0
	v_pk_max_i16 v75, v75, 0
	v_pk_max_i16 v76, v76, 0
	v_pk_max_i16 v77, v77, 0
	s_waitcnt lgkmcnt(0)
	v_mfma_f32_32x32x16_bf16 v[50:65], v[90:93], v[66:69], v[50:65]
	ds_read_b128 v[66:69], v212 offset:24576
	v_mfma_f32_32x32x16_bf16 v[34:49], v[90:93], v[78:81], v[34:49]
	ds_read_b128 v[102:105], v212 offset:7168
	v_mfma_f32_32x32x16_bf16 v[2:17], v[86:89], v[74:77], v[2:17]
	s_waitcnt lgkmcnt(1)
	v_mfma_f32_32x32x16_bf16 v[50:65], v[66:69], v[74:77], v[50:65]
	ds_read_b128 v[74:77], v174 offset:33184
	ds_read_b128 v[78:81], v174 offset:33216
	v_mfma_f32_32x32x16_bf16 v[34:49], v[66:69], v[94:97], v[34:49]
	ds_read_b128 v[66:69], v212 offset:8192
	v_mfma_f32_32x32x16_bf16 v[18:33], v[86:89], v[94:97], v[18:33]
	s_waitcnt lgkmcnt(1)
	v_mfma_f32_32x32x16_bf16 v[86:101], v[102:105], v[126:129], v[70:85]
	v_mfma_f32_32x32x16_bf16 v[70:85], v[102:105], v[134:137], v[70:85]
	ds_read_b128 v[102:105], v212 offset:9216
	v_lshlrev_b32_e32 v135, 2, v1
	v_add_u32_e32 v134, v172, v174
	s_waitcnt lgkmcnt(1)
	v_mfma_f32_32x32x16_bf16 v[86:101], v[66:69], v[122:125], v[86:101]
	v_mfma_f32_32x32x16_bf16 v[70:85], v[66:69], v[146:149], v[70:85]
	ds_read_b128 v[66:69], v212 offset:10240
	s_waitcnt lgkmcnt(1)
	v_mfma_f32_32x32x16_bf16 v[86:101], v[102:105], v[130:133], v[86:101]
	v_mfma_f32_32x32x16_bf16 v[70:85], v[102:105], v[142:145], v[70:85]
	ds_read_b128 v[102:105], v212 offset:17408
	s_waitcnt lgkmcnt(1)
	v_mfma_f32_32x32x16_bf16 v[86:101], v[66:69], v[118:121], v[86:101]
	v_mfma_f32_32x32x16_bf16 v[70:85], v[66:69], v[138:141], v[70:85]
	s_nop 10
	v_cvt_pk_bf16_f32 v68, v90, v91
	v_cvt_pk_bf16_f32 v69, v92, v93
	ds_read_b128 v[90:93], v212 offset:25600
	v_cvt_pk_bf16_f32 v66, v86, v87
	v_cvt_pk_bf16_f32 v67, v88, v89
	v_pk_max_i16 v66, v66, 0
	v_pk_max_i16 v67, v67, 0
	v_pk_max_i16 v68, v68, 0
	v_pk_max_i16 v69, v69, 0
	v_cvt_pk_bf16_f32 v70, v70, v71
	v_cvt_pk_bf16_f32 v71, v72, v73
	s_waitcnt lgkmcnt(1)
	v_mfma_f32_32x32x16_bf16 v[2:17], v[102:105], v[66:69], v[2:17]
	v_cvt_pk_bf16_f32 v72, v74, v75
	v_cvt_pk_bf16_f32 v73, v76, v77
	ds_read_b128 v[74:77], v212 offset:18432
	v_cvt_pk_bf16_f32 v86, v94, v95
	v_cvt_pk_bf16_f32 v87, v96, v97
	v_cvt_pk_bf16_f32 v88, v98, v99
	s_waitcnt lgkmcnt(1)
	v_mfma_f32_32x32x16_bf16 v[50:65], v[90:93], v[66:69], v[50:65]
	ds_read_b128 v[66:69], v212 offset:26624
	v_cvt_pk_bf16_f32 v89, v100, v101
	v_pk_max_i16 v86, v86, 0
	v_pk_max_i16 v87, v87, 0
	v_pk_max_i16 v88, v88, 0
	v_pk_max_i16 v89, v89, 0
	v_pk_max_i16 v70, v70, 0
	v_pk_max_i16 v71, v71, 0
	v_pk_max_i16 v72, v72, 0
	v_pk_max_i16 v73, v73, 0
	v_cvt_pk_bf16_f32 v78, v78, v79
	v_cvt_pk_bf16_f32 v79, v80, v81
	s_waitcnt lgkmcnt(1)
	v_mfma_f32_32x32x16_bf16 v[2:17], v[74:77], v[86:89], v[2:17]
	v_cvt_pk_bf16_f32 v80, v82, v83
	v_cvt_pk_bf16_f32 v81, v84, v85
	v_pk_max_i16 v78, v78, 0
	v_pk_max_i16 v79, v79, 0
	v_pk_max_i16 v80, v80, 0
	v_pk_max_i16 v81, v81, 0
	s_waitcnt lgkmcnt(0)
	v_mfma_f32_32x32x16_bf16 v[50:65], v[66:69], v[86:89], v[50:65]
	v_mfma_f32_32x32x16_bf16 v[34:49], v[90:93], v[70:73], v[34:49]
	s_nop 10
	v_add_f32_e32 v130, v10, v58
	v_add_f32_e32 v131, v11, v59
	v_add_f32_e32 v132, v12, v60
	v_add_f32_e32 v133, v13, v61
	v_add_f32_e32 v138, v4, v52
	v_add_f32_e32 v139, v5, v53
	v_pk_add_f32 v[140:141], v[16:17], v[64:65]
	v_pk_add_f32 v[142:143], v[8:9], v[56:57]
	v_pk_add_f32 v[144:145], v[14:15], v[62:63]
	v_pk_add_f32 v[146:147], v[6:7], v[54:55]
	v_mfma_f32_32x32x16_bf16 v[18:33], v[102:105], v[70:73], v[18:33]
	ds_read2st64_b32 v[70:71], v135 offset0:133 offset1:134
	v_add_f32_e32 v148, v2, v50
	v_add_f32_e32 v149, v3, v51
	v_add_f32_e32 v144, v146, v144
	v_add_f32_e32 v145, v147, v145
	v_pk_add_f32 v[140:141], v[142:143], v[140:141]
	v_pk_add_f32 v[132:133], v[138:139], v[132:133]
	v_pk_add_f32 v[130:131], v[148:149], v[130:131]
	v_pk_add_f32 v[132:133], v[132:133], v[140:141]
	v_pk_add_f32 v[130:131], v[130:131], v[144:145]
	v_mfma_f32_32x32x16_bf16 v[34:49], v[66:69], v[78:81], v[34:49]
	s_waitcnt vmcnt(0) lgkmcnt(0)
	v_mul_f32_e32 v66, v175, v70
	v_add_f32_e32 v130, v131, v130
	v_add_f32_e32 v131, v132, v133
	ds_write_b32 v173, v66 offset:512
	v_mul_f32_e32 v66, v175, v71
	v_add_f32_e32 v130, v130, v131
	s_waitcnt lgkmcnt(0)
	ds_read_b128 v[102:105], v174 offset:34560
	ds_read_b128 v[98:101], v174 offset:34592
	ds_read_b128 v[110:113], v174 offset:34624
	ds_read_b128 v[106:109], v174 offset:34656
	ds_read_b128 v[114:117], v174 offset:34688
	ds_read_b128 v[122:125], v174 offset:34720
	ds_read_b128 v[118:121], v174 offset:34752
	ds_read_b128 v[126:129], v174 offset:34784
	v_mov_b32_dpp v66, v66 quad_perm:[1,0,3,2] row_mask:0xf bank_mask:0xf bound_ctrl:1
	v_mov_b32_e32 v131, v130
	v_fmac_f32_e32 v66, v175, v71
	s_nop 0
	v_permlane32_swap_b32_e32 v130, v131
	v_add_f32_dpp v66, v66, v66 quad_perm:[2,3,0,1] row_mask:0xf bank_mask:0xf bound_ctrl:1
	v_add_f32_e32 v130, v130, v131
	v_fmamk_f32 v65, v130, 0xbc800000, v65
	v_add_f32_dpp v66, v66, v66 row_half_mirror row_mask:0xf bank_mask:0xf bound_ctrl:1
	v_fmamk_f32 v64, v130, 0xbc800000, v64
	v_fmamk_f32 v63, v130, 0xbc800000, v63
	v_fmamk_f32 v62, v130, 0xbc800000, v62
	v_fmamk_f32 v61, v130, 0xbc800000, v61
	v_fmamk_f32 v60, v130, 0xbc800000, v60
	v_fmamk_f32 v59, v130, 0xbc800000, v59
	v_fmamk_f32 v58, v130, 0xbc800000, v58
	v_fmamk_f32 v57, v130, 0xbc800000, v57
	v_fmamk_f32 v56, v130, 0xbc800000, v56
	v_fmamk_f32 v55, v130, 0xbc800000, v55
	v_fmamk_f32 v54, v130, 0xbc800000, v54
	v_fmamk_f32 v53, v130, 0xbc800000, v53
	v_fmamk_f32 v52, v130, 0xbc800000, v52
	v_fmamk_f32 v51, v130, 0xbc800000, v51
	v_fmac_f32_e32 v50, 0xbc800000, v130
	v_add_f32_dpp v66, v66, v66 row_ror:8 row_mask:0xf bank_mask:0xf bound_ctrl:1
	v_fmamk_f32 v17, v130, 0xbc800000, v17
	v_fmamk_f32 v16, v130, 0xbc800000, v16
	v_fmamk_f32 v15, v130, 0xbc800000, v15
	v_fmamk_f32 v14, v130, 0xbc800000, v14
	v_fmamk_f32 v13, v130, 0xbc800000, v13
	v_fmamk_f32 v12, v130, 0xbc800000, v12
	v_fmamk_f32 v11, v130, 0xbc800000, v11
	v_fmamk_f32 v10, v130, 0xbc800000, v10
	v_fmamk_f32 v9, v130, 0xbc800000, v9
	v_fmamk_f32 v8, v130, 0xbc800000, v8
	v_fmamk_f32 v7, v130, 0xbc800000, v7
	v_fmamk_f32 v6, v130, 0xbc800000, v6
	v_fmamk_f32 v5, v130, 0xbc800000, v5
	v_fmamk_f32 v4, v130, 0xbc800000, v4
	v_fmamk_f32 v3, v130, 0xbc800000, v3
	v_fmac_f32_e32 v2, 0xbc800000, v130
	v_pk_mul_f32 v[130:131], v[54:55], v[54:55]
	v_pk_mul_f32 v[132:133], v[62:63], v[62:63]
	v_pk_mul_f32 v[138:139], v[50:51], v[50:51]
	v_pk_mul_f32 v[140:141], v[58:59], v[58:59]
	v_pk_mul_f32 v[142:143], v[56:57], v[56:57]
	v_pk_mul_f32 v[144:145], v[64:65], v[64:65]
	v_pk_mul_f32 v[146:147], v[52:53], v[52:53]
	v_pk_mul_f32 v[148:149], v[60:61], v[60:61]
	v_mov_b32_e32 v67, v66
	v_pk_fma_f32 v[148:149], v[12:13], v[12:13], v[148:149]
	v_pk_fma_f32 v[146:147], v[4:5], v[4:5], v[146:147]
	v_pk_fma_f32 v[144:145], v[16:17], v[16:17], v[144:145]
	v_pk_fma_f32 v[142:143], v[8:9], v[8:9], v[142:143]
	v_pk_fma_f32 v[140:141], v[10:11], v[10:11], v[140:141]
	v_pk_fma_f32 v[138:139], v[2:3], v[2:3], v[138:139]
	v_pk_fma_f32 v[132:133], v[14:15], v[14:15], v[132:133]
	v_pk_fma_f32 v[130:131], v[6:7], v[6:7], v[130:131]
	v_permlane16_swap_b32_e32 v66, v67
	v_pk_add_f32 v[130:131], v[130:131], v[132:133]
	v_pk_add_f32 v[132:133], v[138:139], v[140:141]
	v_pk_add_f32 v[138:139], v[142:143], v[144:145]
	v_pk_add_f32 v[140:141], v[146:147], v[148:149]
	v_mfma_f32_32x32x16_bf16 v[18:33], v[74:77], v[78:81], v[18:33]
	v_add_f32_e32 v136, v66, v67
	ds_read_b128 v[70:73], v134 offset:512
	ds_read_b128 v[66:69], v134 offset:544
	ds_read_b128 v[78:81], v134 offset:576
	ds_read_b128 v[74:77], v134 offset:608
	ds_read_b128 v[82:85], v134 offset:640
	ds_read_b128 v[90:93], v134 offset:672
	ds_read_b128 v[86:89], v134 offset:704
	ds_read_b128 v[94:97], v134 offset:736
	v_pk_add_f32 v[138:139], v[140:141], v[138:139]
	v_pk_add_f32 v[130:131], v[132:133], v[130:131]
	s_waitcnt lgkmcnt(8)
	v_pk_mul_f32 v[140:141], v[126:127], v[62:63]
	v_pk_mov_b32 v[132:133], v[130:131], v[138:139] op_sel:[1,0]
	v_mov_b32_e32 v131, v139
	v_pk_mul_f32 v[138:139], v[122:123], v[54:55]
	v_pk_mul_f32 v[142:143], v[114:115], v[50:51]
	v_pk_mul_f32 v[144:145], v[118:119], v[58:59]
	v_pk_mul_f32 v[146:147], v[124:125], v[56:57]
	v_pk_mul_f32 v[148:149], v[128:129], v[64:65]
	v_pk_mul_f32 v[154:155], v[116:117], v[52:53]
	v_pk_mul_f32 v[156:157], v[120:121], v[60:61]
	v_pk_fma_f32 v[154:155], v[104:105], v[4:5], v[154:155]
	v_pk_fma_f32 v[156:157], v[112:113], v[12:13], v[156:157]
	v_pk_fma_f32 v[148:149], v[108:109], v[16:17], v[148:149]
	v_pk_fma_f32 v[146:147], v[100:101], v[8:9], v[146:147]
	v_pk_fma_f32 v[144:145], v[110:111], v[10:11], v[144:145]
	v_pk_fma_f32 v[142:143], v[102:103], v[2:3], v[142:143]
	v_pk_fma_f32 v[140:141], v[106:107], v[14:15], v[140:141]
	v_pk_fma_f32 v[138:139], v[98:99], v[6:7], v[138:139]
	v_pk_add_f32 v[130:131], v[132:133], v[130:131]
	v_pk_add_f32 v[138:139], v[138:139], v[140:141]
	v_pk_add_f32 v[140:141], v[142:143], v[144:145]
	v_pk_add_f32 v[142:143], v[146:147], v[148:149]
	v_pk_add_f32 v[144:145], v[154:155], v[156:157]
	v_pk_add_f32 v[132:133], v[130:131], v[130:131] op_sel:[0,1] op_sel_hi:[1,0]
	v_pk_add_f32 v[142:143], v[144:145], v[142:143]
	v_pk_add_f32 v[138:139], v[140:141], v[138:139]
	v_add_f32_e32 v133, v142, v143
	v_add_f32_e32 v130, v138, v139
	s_waitcnt lgkmcnt(2)
	v_pk_mul_f32 v[138:139], v[90:91], v[54:55]
	s_waitcnt lgkmcnt(0)
	v_pk_mul_f32 v[140:141], v[94:95], v[62:63]
	v_pk_mul_f32 v[142:143], v[82:83], v[50:51]
	v_pk_mul_f32 v[144:145], v[86:87], v[58:59]
	v_pk_mul_f32 v[146:147], v[92:93], v[56:57]
	v_pk_mul_f32 v[148:149], v[96:97], v[64:65]
	v_pk_mul_f32 v[154:155], v[84:85], v[52:53]
	v_pk_mul_f32 v[156:157], v[88:89], v[60:61]
	v_add_f32_e32 v130, v130, v133
	v_pk_fma_f32 v[156:157], v[80:81], v[12:13], v[156:157]
	v_pk_fma_f32 v[154:155], v[72:73], v[4:5], v[154:155]
	v_pk_fma_f32 v[148:149], v[76:77], v[16:17], v[148:149]
	v_pk_fma_f32 v[146:147], v[68:69], v[8:9], v[146:147]
	v_pk_fma_f32 v[144:145], v[78:79], v[10:11], v[144:145]
	v_pk_fma_f32 v[142:143], v[70:71], v[2:3], v[142:143]
	v_pk_fma_f32 v[140:141], v[74:75], v[14:15], v[140:141]
	v_pk_fma_f32 v[138:139], v[66:67], v[6:7], v[138:139]
	v_mov_b32_e32 v133, v130
	v_pk_add_f32 v[138:139], v[138:139], v[140:141]
	v_pk_add_f32 v[140:141], v[142:143], v[144:145]
	v_pk_add_f32 v[142:143], v[146:147], v[148:149]
	v_pk_add_f32 v[144:145], v[154:155], v[156:157]
	v_permlane32_swap_b32_e32 v130, v133
	v_pk_add_f32 v[142:143], v[144:145], v[142:143]
	v_add_f32_e32 v160, v130, v133
	v_pk_add_f32 v[138:139], v[140:141], v[138:139]
	v_add_f32_e32 v133, v142, v143
	v_pk_add_f32 v[140:141], v[26:27], v[42:43]
	v_pk_add_f32 v[142:143], v[28:29], v[44:45]
	v_pk_add_f32 v[144:145], v[20:21], v[36:37]
	v_pk_add_f32 v[146:147], v[32:33], v[48:49]
	v_pk_add_f32 v[148:149], v[24:25], v[40:41]
	v_pk_add_f32 v[154:155], v[30:31], v[46:47]
	v_pk_add_f32 v[156:157], v[22:23], v[38:39]
	v_pk_add_f32 v[158:159], v[18:19], v[34:35]
	v_pk_add_f32 v[154:155], v[156:157], v[154:155]
	v_pk_add_f32 v[146:147], v[148:149], v[146:147]
	v_pk_add_f32 v[142:143], v[144:145], v[142:143]
	v_pk_add_f32 v[140:141], v[158:159], v[140:141]
	v_pk_add_f32 v[142:143], v[142:143], v[146:147]
	v_pk_add_f32 v[140:141], v[140:141], v[154:155]
	v_add_f32_e32 v130, v138, v139
	v_add_f32_e32 v140, v141, v140
	v_add_f32_e32 v141, v142, v143
	v_add_f32_e32 v133, v130, v133
	v_add_f32_e32 v140, v140, v141
	v_mov_b32_e32 v131, v132
	v_mov_b32_e32 v130, v140
	s_nop 1
	v_permlane32_swap_b32_e32 v140, v130
	v_add_f32_e32 v130, v140, v130
	v_fmamk_f32 v49, v130, 0xbc800000, v49
	v_fmamk_f32 v48, v130, 0xbc800000, v48
	v_fmamk_f32 v47, v130, 0xbc800000, v47
	v_fmamk_f32 v46, v130, 0xbc800000, v46
	v_fmamk_f32 v45, v130, 0xbc800000, v45
	v_fmamk_f32 v44, v130, 0xbc800000, v44
	v_fmamk_f32 v43, v130, 0xbc800000, v43
	v_fmamk_f32 v42, v130, 0xbc800000, v42
	v_fmamk_f32 v41, v130, 0xbc800000, v41
	v_fmamk_f32 v40, v130, 0xbc800000, v40
	v_fmamk_f32 v39, v130, 0xbc800000, v39
	v_fmamk_f32 v38, v130, 0xbc800000, v38
	v_fmamk_f32 v37, v130, 0xbc800000, v37
	v_fmamk_f32 v36, v130, 0xbc800000, v36
	v_fmamk_f32 v35, v130, 0xbc800000, v35
	v_fmac_f32_e32 v34, 0xbc800000, v130
	v_fmamk_f32 v33, v130, 0xbc800000, v33
	v_fmamk_f32 v32, v130, 0xbc800000, v32
	v_fmamk_f32 v31, v130, 0xbc800000, v31
	v_fmamk_f32 v30, v130, 0xbc800000, v30
	v_fmamk_f32 v29, v130, 0xbc800000, v29
	v_fmamk_f32 v28, v130, 0xbc800000, v28
	v_fmamk_f32 v27, v130, 0xbc800000, v27
	v_fmamk_f32 v26, v130, 0xbc800000, v26
	v_fmamk_f32 v25, v130, 0xbc800000, v25
	v_fmamk_f32 v24, v130, 0xbc800000, v24
	v_fmamk_f32 v23, v130, 0xbc800000, v23
	v_fmamk_f32 v22, v130, 0xbc800000, v22
	v_fmamk_f32 v21, v130, 0xbc800000, v21
	v_fmamk_f32 v20, v130, 0xbc800000, v20
	v_fmamk_f32 v19, v130, 0xbc800000, v19
	v_fmac_f32_e32 v18, 0xbc800000, v130
	v_pk_mul_f32 v[140:141], v[38:39], v[38:39]
	v_pk_mul_f32 v[142:143], v[46:47], v[46:47]
	v_pk_mul_f32 v[144:145], v[34:35], v[34:35]
	v_pk_mul_f32 v[146:147], v[42:43], v[42:43]
	v_pk_mul_f32 v[148:149], v[40:41], v[40:41]
	v_pk_mul_f32 v[154:155], v[48:49], v[48:49]
	v_pk_mul_f32 v[156:157], v[36:37], v[36:37]
	v_pk_mul_f32 v[158:159], v[44:45], v[44:45]
	v_pk_fma_f32 v[156:157], v[20:21], v[20:21], v[156:157]
	v_pk_fma_f32 v[158:159], v[28:29], v[28:29], v[158:159]
	v_pk_fma_f32 v[154:155], v[32:33], v[32:33], v[154:155]
	v_pk_fma_f32 v[148:149], v[24:25], v[24:25], v[148:149]
	v_pk_fma_f32 v[146:147], v[26:27], v[26:27], v[146:147]
	v_pk_fma_f32 v[144:145], v[18:19], v[18:19], v[144:145]
	v_pk_fma_f32 v[142:143], v[30:31], v[30:31], v[142:143]
	v_pk_fma_f32 v[140:141], v[22:23], v[22:23], v[140:141]
	v_permlane32_swap_b32_e32 v132, v131
	v_pk_add_f32 v[140:141], v[140:141], v[142:143]
	v_pk_add_f32 v[142:143], v[144:145], v[146:147]
	v_pk_add_f32 v[144:145], v[148:149], v[154:155]
	v_pk_add_f32 v[146:147], v[156:157], v[158:159]
	v_pk_add_f32 v[140:141], v[142:143], v[140:141]
	v_pk_add_f32 v[144:145], v[146:147], v[144:145]
	v_pk_mul_f32 v[122:123], v[122:123], v[38:39]
	v_pk_mov_b32 v[142:143], v[140:141], v[144:145] op_sel:[1,0]
	v_mov_b32_e32 v141, v145
	v_pk_add_f32 v[140:141], v[142:143], v[140:141]
	v_pk_mul_f32 v[126:127], v[126:127], v[46:47]
	v_pk_add_f32 v[140:141], v[140:141], v[140:141] op_sel:[0,1] op_sel_hi:[1,0]
	v_pk_mul_f32 v[114:115], v[114:115], v[34:35]
	v_mov_b32_e32 v130, v140
	s_nop 1
	v_permlane32_swap_b32_e32 v140, v130
	v_mov_b32_e32 v141, v132
	v_pk_add_f32 v[130:131], v[140:141], v[130:131]
	v_pk_mul_f32 v[118:119], v[118:119], v[42:43]
	v_pk_fma_f32 v[130:131], v[130:131], s[0:1], v[152:153] op_sel_hi:[1,0,0]
	v_pk_mul_f32 v[124:125], v[124:125], v[40:41]
	v_pk_mul_f32 v[128:129], v[128:129], v[48:49]
	v_pk_mul_f32 v[116:117], v[116:117], v[36:37]
	v_pk_mul_f32 v[120:121], v[120:121], v[44:45]
	v_pk_fma_f32 v[112:113], v[112:113], v[28:29], v[120:121]
	v_pk_fma_f32 v[104:105], v[104:105], v[20:21], v[116:117]
	v_pk_fma_f32 v[108:109], v[108:109], v[32:33], v[128:129]
	v_pk_fma_f32 v[100:101], v[100:101], v[24:25], v[124:125]
	v_pk_fma_f32 v[110:111], v[110:111], v[26:27], v[118:119]
	v_pk_fma_f32 v[102:103], v[102:103], v[18:19], v[114:115]
	v_pk_fma_f32 v[106:107], v[106:107], v[30:31], v[126:127]
	v_pk_fma_f32 v[98:99], v[98:99], v[22:23], v[122:123]
	v_rsq_f32_e32 v131, v131
	v_pk_add_f32 v[98:99], v[98:99], v[106:107]
	v_pk_add_f32 v[102:103], v[102:103], v[110:111]
	v_pk_add_f32 v[100:101], v[100:101], v[108:109]
	v_pk_add_f32 v[104:105], v[104:105], v[112:113]
	v_rsq_f32_e32 v132, v130
	v_pk_add_f32 v[100:101], v[104:105], v[100:101]
	v_pk_add_f32 v[98:99], v[102:103], v[98:99]
	v_add_f32_e32 v98, v98, v99
	v_add_f32_e32 v99, v100, v101
	v_add_f32_e32 v98, v98, v99
	v_mov_b32_e32 v99, v98
	v_pk_mul_f32 v[90:91], v[90:91], v[38:39]
	v_pk_mul_f32 v[94:95], v[94:95], v[46:47]
	v_pk_mul_f32 v[82:83], v[82:83], v[34:35]
	v_pk_mul_f32 v[86:87], v[86:87], v[42:43]
	v_permlane32_swap_b32_e32 v98, v99
	v_pk_fma_f32 v[78:79], v[78:79], v[26:27], v[86:87]
	v_pk_fma_f32 v[70:71], v[70:71], v[18:19], v[82:83]
	v_pk_fma_f32 v[74:75], v[74:75], v[30:31], v[94:95]
	v_pk_fma_f32 v[66:67], v[66:67], v[22:23], v[90:91]
	v_mov_b32_e32 v130, v131
	v_mov_b32_e32 v131, v132
	v_add_f32_e32 v98, v98, v99
	v_pk_add_f32 v[66:67], v[66:67], v[74:75]
	v_pk_add_f32 v[70:71], v[70:71], v[78:79]
	v_mul_f32_e32 v139, v160, v130
	v_mul_f32_e32 v98, v98, v131
	v_pk_add_f32 v[66:67], v[70:71], v[66:67]
	v_cmp_gt_u32_e32 vcc, 32, v1
	v_add_f32_e32 v66, v66, v67
	v_pk_mul_f32 v[92:93], v[92:93], v[40:41]
	v_cndmask_b32_e32 v67, v98, v139, vcc
	v_add_f32_e32 v67, s12, v67
	v_pk_mul_f32 v[96:97], v[96:97], v[48:49]
	v_pk_mul_f32 v[84:85], v[84:85], v[36:37]
	v_pk_mul_f32 v[88:89], v[88:89], v[44:45]
	v_mul_f32_e32 v67, 0xbfb8aa3b, v67
	v_pk_fma_f32 v[80:81], v[80:81], v[28:29], v[88:89]
	v_pk_fma_f32 v[72:73], v[72:73], v[20:21], v[84:85]
	v_pk_fma_f32 v[76:77], v[76:77], v[32:33], v[96:97]
	v_pk_fma_f32 v[68:69], v[68:69], v[24:25], v[92:93]
	v_exp_f32_e32 v70, v67
	v_pk_add_f32 v[68:69], v[68:69], v[76:77]
	v_pk_add_f32 v[72:73], v[72:73], v[80:81]
	v_cmp_lt_i32_e64 s[0:1], 0, v151
	v_pk_add_f32 v[68:69], v[72:73], v[68:69]
	v_mov_b32_e32 v137, v136
	v_add_f32_e32 v67, v68, v69
	v_add_f32_e32 v67, v66, v67
	v_add_f32_e32 v66, 1.0, v70
	v_rcp_f32_e32 v66, v66
	v_mov_b32_e32 v69, 0xff800000
	v_mov_b32_e32 v138, v133
	v_mov_b32_e32 v68, v67
	v_cndmask_b32_e64 v70, v69, v66, s[0:1]
	v_mbcnt_lo_u32_b32 v66, -1, 0
	v_mbcnt_hi_u32_b32 v66, -1, v66
	v_permlane32_swap_b32_e32 v136, v137
	v_permlane32_swap_b32_e32 v133, v138
	v_permlane32_swap_b32_e32 v67, v68
	v_and_b32_e32 v86, 64, v66
	s_mov_b32 s14, 8
	s_mov_b32 s13, 0
	v_mov_b32_e32 v66, 0
	s_waitcnt lgkmcnt(0)
